# GDN a+b: 52 prefetch hand-off register copies per item coalesced away (readers name the prefetch registers directly)
# speedup vs baseline: 1.0034x; 1.0030x over previous
.LBB0_221:
	s_memrealtime s[0:1]
	s_waitcnt vmcnt(8)
	s_lshl_b32 s100, s76, 4
	s_lshl_b32 s2, s76, 6
	s_and_b32 s100, s100, 0xfffff000
	s_and_b32 s2, s2, 0xfc0
	v_mov_b32_e32 v215, v237
	v_mov_b32_e32 v216, v236
	s_or_b32 s100, s100, s2
	v_readlane_b32 s20, v253, 23
	s_bfe_u32 s101, s76, 0x20006
	v_readlane_b32 s21, v253, 24
	s_lshl_b32 s74, s101, 2
	s_nop 0
	v_lshlrev_b32_e32 v38, 1, v215
	v_readlane_b32 s20, v253, 27
	v_readlane_b32 s21, v253, 28
	v_readlane_b32 s20, v253, 29
	v_readlane_b32 s21, v253, 30
	s_not_b32 s101, s2
	v_readlane_b32 s20, v253, 31
	v_readlane_b32 s21, v253, 32
	s_nop 0
	v_readlane_b32 s20, v253, 33
	v_readlane_b32 s21, v253, 34
	s_cmp_le_i32 s31, s101
	v_mov_b32_e32 v27, v141
	v_readlane_b32 s20, v253, 35
	v_readlane_b32 s21, v253, 36
	s_nop 1
	v_readlane_b32 s20, v253, 37
	v_readlane_b32 s21, v253, 38
	s_nop 1
	v_readlane_b32 s20, v253, 39
	v_readlane_b32 s21, v253, 40
	s_nop 0
	s_nop 0
	s_nop 0
	s_nop 0
	s_nop 0
	s_nop 0
	v_mov_b32_e32 v28, v141
	v_mov_b32_e32 v29, v141
	s_cbranch_scc1 .LBB0_223
	s_add_i32 s2, s100, s31
	s_ashr_i32 s3, s2, 31
	s_lshl_b64 s[2:3], s[2:3], 9
	v_mov_b32_e32 v27, v172
	v_mov_b32_e32 v28, v173
	s_nop 0
	v_mov_b32_e32 v29, v174

.LBB0_227:
	s_add_i32 s2, s100, s95
	s_ashr_i32 s3, s2, 31
	s_lshl_b64 s[2:3], s[2:3], 9
	s_add_i32 s2, s100, s54
	s_ashr_i32 s3, s2, 31
	s_lshl_b64 s[2:3], s[2:3], 9
	s_nop 0
	s_add_i32 s2, s100, s55
	s_ashr_i32 s3, s2, 31
	s_lshl_b64 s[2:3], s[2:3], 9
	s_nop 0
	s_add_i32 s2, s100, s33
	s_ashr_i32 s3, s2, 31
	s_lshl_b64 s[2:3], s[2:3], 9
	s_nop 0
	s_nop 0
	s_add_i32 s2, s100, s4
	s_ashr_i32 s3, s2, 31
	s_lshl_b64 s[2:3], s[2:3], 9
	s_nop 0
	s_add_i32 s2, s100, s5
	s_ashr_i32 s3, s2, 31
	s_lshl_b64 s[2:3], s[2:3], 9
	s_nop 0
	s_nop 0
	s_add_i32 s2, s100, s6
	s_ashr_i32 s3, s2, 31
	s_lshl_b64 s[2:3], s[2:3], 9
	s_add_i32 s100, s100, s7
	s_ashr_i32 s101, s100, 31
	s_lshl_b64 s[100:101], s[100:101], 9
	s_waitcnt lgkmcnt(0)
	v_add_f32_e32 v24, v206, v220
	s_mov_b32 s0, 0x41a00000
	v_cmp_nlt_f32_e32 vcc, s0, v24
	s_and_saveexec_b64 s[0:1], vcc
	s_cbranch_execz .LBB0_229
	v_mul_f32_e32 v24, 0x3fb8aa3b, v24
	v_exp_f32_e32 v68, v24
	s_mov_b32 s2, 0x3f2aaaab
	v_add_f32_e32 v54, 1.0, v68
	v_frexp_mant_f32_e32 v58, v54
	v_cvt_f64_f32_e32 v[24:25], v54
	v_frexp_exp_i32_f64_e32 v24, v[24:25]
	v_cmp_gt_f32_e32 vcc, s2, v58
	v_add_f32_e32 v55, -1.0, v54
	v_sub_f32_e32 v59, v55, v54
	v_subbrev_co_u32_e32 v62, vcc, 0, v24, vcc
	v_sub_u32_e32 v24, 0, v62
	v_sub_f32_e32 v55, v68, v55
	v_add_f32_e32 v59, 1.0, v59
	v_ldexp_f32 v25, v54, v24
	v_add_f32_e32 v55, v55, v59
	v_add_f32_e32 v54, -1.0, v25
	v_add_f32_e32 v58, 1.0, v25
	v_ldexp_f32 v24, v55, v24
	v_add_f32_e32 v55, 1.0, v54
	v_add_f32_e32 v59, -1.0, v58
	v_sub_f32_e32 v55, v25, v55
	v_sub_f32_e32 v25, v25, v59
	v_add_f32_e32 v55, v24, v55
	v_add_f32_e32 v24, v24, v25
	v_add_f32_e32 v63, v58, v24
	v_rcp_f32_e32 v65, v63
	v_sub_f32_e32 v25, v63, v58
	v_sub_f32_e32 v64, v24, v25
	v_add_f32_e32 v25, v54, v55
	v_mul_f32_e32 v67, v25, v65
	v_sub_f32_e32 v24, v25, v54
	v_mul_f32_e32 v54, v63, v67
	v_fma_f32 v58, v67, v63, -v54
	v_fmac_f32_e32 v58, v67, v64
	v_sub_f32_e32 v66, v55, v24
	v_add_f32_e32 v24, v54, v58
	v_sub_f32_e32 v55, v25, v24
	v_pk_add_f32 v[60:61], v[24:25], v[54:55] neg_lo:[0,1] neg_hi:[0,1]
	v_mov_b32_e32 v59, v24
	v_pk_add_f32 v[24:25], v[60:61], v[58:59] neg_lo:[0,1] neg_hi:[0,1]
	s_mov_b32 s2, 0x3f317218
	v_add_f32_e32 v25, v66, v25
	v_add_f32_e32 v24, v24, v25
	v_add_f32_e32 v25, v55, v24
	v_mul_f32_e32 v66, v65, v25
	v_mul_f32_e32 v54, v63, v66
	v_fma_f32 v58, v66, v63, -v54
	v_fmac_f32_e32 v58, v66, v64
	v_sub_f32_e32 v55, v55, v25
	v_add_f32_e32 v63, v24, v55
	v_add_f32_e32 v24, v54, v58
	v_sub_f32_e32 v55, v25, v24
	v_pk_add_f32 v[60:61], v[24:25], v[54:55] neg_lo:[0,1] neg_hi:[0,1]
	v_mov_b32_e32 v59, v24
	v_pk_add_f32 v[24:25], v[60:61], v[58:59] neg_lo:[0,1] neg_hi:[0,1]
	s_nop 0
	v_add_f32_e32 v25, v63, v25
	v_add_f32_e32 v24, v24, v25
	v_add_f32_e32 v25, v67, v66
	v_add_f32_e32 v24, v55, v24
	v_sub_f32_e32 v54, v25, v67
	v_mul_f32_e32 v24, v65, v24
	v_sub_f32_e32 v54, v66, v54
	v_add_f32_e32 v54, v54, v24
	v_add_f32_e32 v58, v25, v54
	v_mul_f32_e32 v59, v58, v58
	v_fmamk_f32 v24, v59, 0x3e9b6dac, v208
	v_fmaak_f32 v143, v59, v24, 0x3f2aaada
	v_cvt_f32_i32_e32 v24, v62
	v_sub_f32_e32 v25, v58, v25
	v_sub_f32_e32 v25, v54, v25
	v_ldexp_f32 v60, v25, 1
	v_mul_f32_e32 v25, v58, v59
	v_ldexp_f32 v55, v58, 1
	v_pk_mul_f32 v[58:59], v[24:25], v[142:143]
	s_nop 0
	v_fma_f32 v54, v24, s2, -v58
	v_fmac_f32_e32 v54, 0xb102e308, v24
	v_pk_add_f32 v[24:25], v[58:59], v[54:55]
	s_mov_b32 s2, 0x7f800000
	v_sub_f32_e32 v55, v25, v55
	v_sub_f32_e32 v55, v59, v55
	v_add_f32_e32 v61, v60, v55
	v_mov_b32_e32 v60, v58
	v_pk_add_f32 v[58:59], v[24:25], v[58:59] neg_lo:[0,1] neg_hi:[0,1]
	v_pk_add_f32 v[62:63], v[24:25], v[60:61]
	v_mov_b32_e32 v55, v24
	v_mov_b32_e32 v59, v63
	v_pk_add_f32 v[64:65], v[54:55], v[58:59] neg_lo:[0,1] neg_hi:[0,1]
	v_pk_add_f32 v[54:55], v[54:55], v[58:59]
	v_mov_b32_e32 v60, v61
	v_pk_add_f32 v[58:59], v[54:55], v[24:25] op_sel:[1,0] op_sel_hi:[0,1] neg_lo:[0,1] neg_hi:[0,1]
	v_pk_add_f32 v[66:67], v[62:63], v[58:59] op_sel_hi:[1,0] neg_lo:[0,1] neg_hi:[0,1]
	v_mov_b32_e32 v62, v63
	v_mov_b32_e32 v63, v55
	v_pk_mov_b32 v[58:59], v[24:25], v[58:59] op_sel:[1,0]
	v_mov_b32_e32 v61, v24
	v_pk_add_f32 v[58:59], v[62:63], v[58:59] neg_lo:[0,1] neg_hi:[0,1]
	v_mov_b32_e32 v66, v64
	v_pk_add_f32 v[24:25], v[60:61], v[58:59] neg_lo:[0,1] neg_hi:[0,1]
	v_mov_b32_e32 v65, v55
	v_pk_add_f32 v[58:59], v[66:67], v[24:25]
	v_cmp_neq_f32_e32 vcc, s2, v68
	v_pk_add_f32 v[60:61], v[58:59], v[58:59] op_sel:[0,1] op_sel_hi:[1,0]
	s_mov_b32 s2, 0x33800000
	v_pk_add_f32 v[54:55], v[54:55], v[60:61] op_sel:[1,0] op_sel_hi:[0,1]
	v_mov_b32_e32 v59, v54
	v_pk_add_f32 v[62:63], v[58:59], v[64:65] neg_lo:[0,1] neg_hi:[0,1]
	v_mov_b32_e32 v25, v60
	v_sub_f32_e32 v55, v58, v62
	v_pk_add_f32 v[24:25], v[24:25], v[62:63] neg_lo:[0,1] neg_hi:[0,1]
	v_sub_f32_e32 v55, v64, v55
	v_add_f32_e32 v24, v24, v55
	v_add_f32_e32 v24, v24, v25
	v_add_f32_e32 v24, v54, v24
	v_cndmask_b32_e32 v24, v211, v24, vcc
	v_cmp_ngt_f32_e32 vcc, -1.0, v68
	s_nop 1
	v_cndmask_b32_e32 v24, v212, v24, vcc
	v_cmp_neq_f32_e32 vcc, -1.0, v68
	s_nop 1
	v_cndmask_b32_e32 v24, v213, v24, vcc
	v_cmp_lt_f32_e64 vcc, |v68|, s2
	s_nop 1
	v_cndmask_b32_e32 v24, v24, v68, vcc
.LBB0_229:
	s_or_b64 exec, exec, s[0:1]
	v_mul_f32_e32 v25, 0x3fb8aa3b, v221
	v_exp_f32_e32 v25, v25
	v_and_b32_e32 v100, 64, v209
	v_mul_f32_e64 v54, v24, -v25
	v_readlane_b32 s0, v253, 41
	v_readlane_b32 s1, v253, 42
	s_ashr_i32 s77, s76, 31
	v_mov_b32_e32 v25, v54
	s_nop 1
	v_add_f32_dpp v25, v25, v25 row_shr:1 row_mask:0xf bank_mask:0xf
	s_nop 1
	v_add_f32_dpp v25, v25, v25 row_shr:2 row_mask:0xf bank_mask:0xf
	s_nop 1
	v_add_f32_dpp v25, v25, v25 row_shr:4 row_mask:0xf bank_mask:0xf
	s_nop 1
	v_add_f32_dpp v25, v25, v25 row_shr:8 row_mask:0xf bank_mask:0xf
	s_nop 1
	v_add_f32_dpp v25, v25, v25 row_bcast:15 row_mask:0xa bank_mask:0xf
	s_nop 1
	v_add_f32_dpp v25, v25, v25 row_bcast:31 row_mask:0xc bank_mask:0xf
	s_nop 1
	v_readlane_b32 s99, v25, 63
	s_nop 1
	v_mov_b32_e32 v24, s99
	v_mul_f32_e32 v34, 0x3fb8aa3b, v25
	v_exp_f32_e32 v94, v34
	s_andn2_b64 vcc, exec, s[0:1]
	s_cbranch_vccnz .LBB0_233
	s_waitcnt lgkmcnt(0)
	v_sub_f32_e32 v34, v24, v25
	v_mul_f32_e32 v34, 0x3fb8aa3b, v34
	v_exp_f32_e32 v34, v34
	v_lshl_add_u32 v54, v215, 2, 0
	v_add_u32_e32 v55, 0x1c400, v54
	ds_write_b32 v55, v25
	v_add_u32_e32 v25, 0x1c600, v54
	ds_write_b32 v25, v94
	v_add_u32_e32 v25, 0x1c700, v54
	v_cmp_eq_u32_e32 vcc, 0, v215
	ds_write_b32 v25, v34
	s_and_saveexec_b64 s[0:1], vcc
	s_cbranch_execz .LBB0_232
	s_lshl_b64 s[2:3], s[76:77], 2
	v_readlane_b32 s20, v253, 25
	s_add_u32 s2, s20, s2
	v_readlane_b32 s20, v253, 26
	s_addc_u32 s3, s20, s3
	global_store_dword v141, v24, s[2:3]

.LBB0_233:
	v_lshlrev_b32_e32 v68, 16, v182
	v_and_b32_e32 v69, 0xffff0000, v182
	v_lshlrev_b32_e32 v74, 16, v185
	v_and_b32_e32 v75, 0xffff0000, v185
	v_xor_b32_e32 v39, 32, v209
	v_add_u32_e32 v42, 64, v100
	v_cmp_lt_i32_e32 vcc, v39, v42
	v_lshlrev_b32_e32 v108, 16, v28
	v_and_b32_e32 v109, 0xffff0000, v28
	v_cndmask_b32_e32 v39, v209, v39, vcc
	v_lshlrev_b32_e32 v105, 2, v39
	v_xor_b32_e32 v39, 16, v209
	v_cmp_lt_i32_e32 vcc, v39, v42
	v_lshlrev_b32_e32 v85, 16, v183
	v_and_b32_e32 v81, 0xffff0000, v183
	v_cndmask_b32_e32 v39, v209, v39, vcc
	v_lshlrev_b32_e32 v103, 2, v39
	v_xor_b32_e32 v39, 8, v209
	v_cmp_lt_i32_e32 vcc, v39, v42
	v_lshlrev_b32_e32 v78, 16, v184
	v_and_b32_e32 v79, 0xffff0000, v184
	v_cndmask_b32_e32 v39, v209, v39, vcc
	v_lshlrev_b32_e32 v102, 2, v39
	v_xor_b32_e32 v39, 4, v209
	v_cmp_lt_i32_e32 vcc, v39, v42
	v_lshlrev_b32_e32 v40, 16, v202
	v_and_b32_e32 v41, 0xffff0000, v202
	v_cndmask_b32_e32 v39, v209, v39, vcc
	v_lshlrev_b32_e32 v101, 2, v39
	v_xor_b32_e32 v39, 2, v209
	v_cmp_lt_i32_e32 vcc, v39, v42
	v_lshl_add_u32 v97, v38, 1, 0
	v_bitop3_b32 v38, v215, s82, 7 bitop3:0x6c
	v_cndmask_b32_e32 v39, v209, v39, vcc
	v_lshlrev_b32_e32 v100, 2, v39
	v_xor_b32_e32 v39, 1, v209
	v_cmp_lt_i32_e32 vcc, v39, v42
	v_lshlrev_b32_e32 v116, 16, v32
	v_and_b32_e32 v117, 0xffff0000, v32
	v_cndmask_b32_e32 v39, v209, v39, vcc
	v_lshlrev_b32_e32 v84, 16, v36
	v_and_b32_e32 v91, 0xffff0000, v36
	v_lshlrev_b32_e32 v58, 16, v35
	v_and_b32_e32 v59, 0xffff0000, v35
	v_lshlrev_b32_e32 v66, 16, v181
	v_and_b32_e32 v67, 0xffff0000, v181
	v_lshlrev_b32_e32 v76, 16, v188
	v_and_b32_e32 v77, 0xffff0000, v188
	v_lshlrev_b32_e32 v54, 16, v190
	v_and_b32_e32 v55, 0xffff0000, v190
	v_lshlrev_b32_e32 v46, 16, v194
	v_and_b32_e32 v47, 0xffff0000, v194
	v_lshlrev_b32_e32 v34, 16, v196
	v_and_b32_e32 v35, 0xffff0000, v196
	v_lshlrev_b32_e32 v36, 16, v199
	v_and_b32_e32 v37, 0xffff0000, v199
	v_lshlrev_b32_e32 v52, 16, v203
	v_and_b32_e32 v53, 0xffff0000, v203
	v_lshlrev_b32_e32 v98, 2, v39
	v_lshlrev_b32_e32 v92, 3, v38
	v_pk_fma_f32 v[38:39], v[224:225], v[108:109], 0 op_sel_hi:[1,1,0]
	v_lshlrev_b32_e32 v62, 16, v30
	v_and_b32_e32 v63, 0xffff0000, v30
	v_pk_fma_f32 v[38:39], v[230:231], v[116:117], v[38:39]
	v_lshlrev_b32_e32 v106, 16, v27
	v_pk_fma_f32 v[38:39], v[238:239], v[62:63], v[38:39]
	v_and_b32_e32 v107, 0xffff0000, v27
	v_pk_fma_f32 v[38:39], v[244:245], v[68:69], v[38:39]
	v_lshlrev_b32_e32 v87, 16, v186
	v_and_b32_e32 v83, 0xffff0000, v186
	v_mul_f32_e32 v42, 0xbfb8aa3b, v38
	v_mul_f32_e32 v43, 0xbfb8aa3b, v39
	v_lshlrev_b32_e32 v114, 16, v31
	v_and_b32_e32 v115, 0xffff0000, v31
	v_lshlrev_b32_e32 v72, 16, v187
	v_and_b32_e32 v73, 0xffff0000, v187
	v_lshlrev_b32_e32 v70, 16, v189
	v_and_b32_e32 v64, 0xffff0000, v189
	v_exp_f32_e32 v42, v42
	v_exp_f32_e32 v43, v43
	v_pk_fma_f32 v[44:45], v[222:223], v[106:107], 0 op_sel_hi:[1,1,0]
	v_lshlrev_b32_e32 v112, 16, v29
	v_pk_fma_f32 v[44:45], v[228:229], v[114:115], v[44:45]
	v_and_b32_e32 v88, 0xffff0000, v29
	v_pk_fma_f32 v[44:45], v[234:235], v[58:59], v[44:45]
	v_lshlrev_b32_e32 v71, 16, v192
	v_pk_fma_f32 v[44:45], v[242:243], v[66:67], v[44:45]
	v_and_b32_e32 v65, 0xffff0000, v192
	v_lshlrev_b32_e32 v60, 16, v191
	v_and_b32_e32 v61, 0xffff0000, v191
	v_lshlrev_b32_e32 v29, 16, v198
	v_and_b32_e32 v25, 0xffff0000, v198
	v_lshlrev_b32_e32 v48, 16, v197
	v_and_b32_e32 v49, 0xffff0000, v197
	v_add_f32_e32 v42, 1.0, v42
	v_add_f32_e32 v43, 1.0, v43
	v_mul_f32_e32 v56, 0xbfb8aa3b, v44
	v_mul_f32_e32 v57, 0xbfb8aa3b, v45
	v_rcp_f32_e32 v42, v42
	v_rcp_f32_e32 v43, v43
	v_exp_f32_e32 v56, v56
	v_exp_f32_e32 v57, v57
	v_lshlrev_b32_e32 v113, 16, v33
	v_pk_mul_f32 v[38:39], v[38:39], v[42:43]
	v_add_f32_e32 v42, 1.0, v56
	v_add_f32_e32 v43, 1.0, v57
	v_rcp_f32_e32 v42, v42
	v_rcp_f32_e32 v43, v43
	v_pk_mul_f32 v[56:57], v[38:39], v[38:39]
	v_mov_b32_e32 v86, v85
	v_add_f32_e32 v119, v56, v57
	v_pk_mul_f32 v[44:45], v[44:45], v[42:43]
	v_pk_fma_f32 v[42:43], v[224:225], v[116:117], 0 op_sel_hi:[1,1,0]
	s_waitcnt lgkmcnt(0)
	v_mul_f32_e32 v24, 0xbfb8aa3b, v205
	v_pk_fma_f32 v[42:43], v[230:231], v[62:63], v[42:43]
	v_exp_f32_e32 v24, v24
	v_pk_fma_f32 v[42:43], v[238:239], v[68:69], v[42:43]
	v_and_b32_e32 v89, 0xffff0000, v33
	v_pk_fma_f32 v[42:43], v[244:245], v[74:75], v[42:43]
	v_add_f32_e32 v24, 1.0, v24
	v_mul_f32_e32 v56, 0xbfb8aa3b, v42
	v_exp_f32_e32 v106, v56
	v_mul_f32_e32 v56, 0xbfb8aa3b, v43
	v_exp_f32_e32 v107, v56
	v_pk_mul_f32 v[56:57], v[44:45], v[44:45]
	v_add_f32_e32 v106, 1.0, v106
	v_rcp_f32_e32 v106, v106
	v_add_f32_e32 v107, 1.0, v107
	v_rcp_f32_e32 v107, v107
	v_add_f32_e32 v116, v56, v57
	v_rcp_f32_e32 v95, v24
	v_mov_b32_e32 v90, v89
	v_pk_mul_f32 v[42:43], v[42:43], v[106:107]
	v_pk_fma_f32 v[88:89], v[226:227], v[88:89], 0 op_sel:[1,0,0] op_sel_hi:[1,1,0]
	v_pk_mul_f32 v[56:57], v[42:43], v[42:43]
	v_mov_b32_e32 v80, v91
	v_add_f32_e32 v117, v56, v57
	v_pk_fma_f32 v[56:57], v[222:223], v[114:115], 0 op_sel_hi:[1,1,0]
	v_mov_b32_e32 v114, v113
	v_pk_fma_f32 v[56:57], v[228:229], v[58:59], v[56:57]
	v_mov_b32_e32 v115, v84
	v_pk_fma_f32 v[56:57], v[234:235], v[66:67], v[56:57]
	v_pk_fma_f32 v[112:113], v[226:227], v[112:113], 0 op_sel_hi:[0,1,0]
	v_pk_fma_f32 v[56:57], v[242:243], v[78:79], v[56:57]
	v_pk_fma_f32 v[112:113], v[232:233], v[114:115], v[112:113] op_sel_hi:[0,1,1]
	v_mul_f32_e32 v106, 0xbfb8aa3b, v56
	v_exp_f32_e32 v107, v106
	v_mul_f32_e32 v106, 0xbfb8aa3b, v57
	v_exp_f32_e32 v109, v106
	v_pk_fma_f32 v[112:113], v[240:241], v[84:85], v[112:113] op_sel_hi:[0,1,1]
	v_add_f32_e32 v107, 1.0, v107
	v_pk_fma_f32 v[112:113], v[246:247], v[86:87], v[112:113] op_sel_hi:[0,1,1]
	v_rcp_f32_e32 v108, v107
	v_add_f32_e32 v107, 1.0, v109
	v_mul_f32_e32 v109, 0xbfb8aa3b, v112
	v_exp_f32_e32 v110, v109
	v_mul_f32_e32 v109, 0xbfb8aa3b, v113
	v_exp_f32_e32 v115, v109
	v_rcp_f32_e32 v109, v107
	v_add_f32_e32 v107, 1.0, v110
	v_rcp_f32_e32 v114, v107
	v_add_f32_e32 v107, 1.0, v115
	v_rcp_f32_e32 v115, v107
	v_pk_mul_f32 v[56:57], v[56:57], v[108:109]
	v_readlane_b32 s2, v95, s95
	v_pk_mul_f32 v[108:109], v[56:57], v[56:57]
	v_readlane_b32 s3, v95, s54
	v_add_f32_e32 v120, v108, v109
	v_pk_mul_f32 v[108:109], v[112:113], v[114:115]
	v_pk_fma_f32 v[88:89], v[232:233], v[90:91], v[88:89] op_sel:[1,0,0]
	v_mov_b32_e32 v82, v81
	v_pk_mul_f32 v[108:109], v[108:109], s[2:3]
	v_pk_fma_f32 v[88:89], v[240:241], v[80:81], v[88:89] op_sel:[1,0,0]
	v_cvt_pk_bf16_f32 v107, v108, v109
	v_pk_fma_f32 v[108:109], v[246:247], v[82:83], v[88:89] op_sel:[1,0,0]
	v_pk_fma_f32 v[62:63], v[224:225], v[62:63], 0 op_sel_hi:[1,1,0]
	v_mul_f32_e32 v88, 0xbfb8aa3b, v108
	v_exp_f32_e32 v88, v88
	v_mul_f32_e32 v89, 0xbfb8aa3b, v109
	v_exp_f32_e32 v89, v89
	v_pk_fma_f32 v[62:63], v[230:231], v[68:69], v[62:63]
	v_lshlrev_b32_e32 v32, 16, v193
	v_and_b32_e32 v33, 0xffff0000, v193
	v_lshlrev_b32_e32 v28, 16, v195
	v_and_b32_e32 v24, 0xffff0000, v195
	v_lshlrev_b32_e32 v50, 16, v200
	v_and_b32_e32 v51, 0xffff0000, v200
	v_mul_lo_u32 v93, v215, s11
	v_add_f32_e32 v88, 1.0, v88
	v_pk_fma_f32 v[62:63], v[238:239], v[74:75], v[62:63]
	v_add_lshl_u32 v90, v92, v93, 1
	v_rcp_f32_e32 v112, v88
	v_add_f32_e32 v88, 1.0, v89
	v_pk_fma_f32 v[62:63], v[244:245], v[76:77], v[62:63]
	v_rcp_f32_e32 v113, v88
	v_add_u32_e32 v88, 0, v90
	v_add_u32_e32 v91, s12, v90
	v_mul_f32_e32 v90, 0xbfb8aa3b, v62
	v_exp_f32_e32 v90, v90
	v_mul_f32_e32 v110, 0xbfb8aa3b, v63
	v_exp_f32_e32 v110, v110
	v_pk_fma_f32 v[58:59], v[222:223], v[58:59], 0 op_sel_hi:[1,1,0]
	v_add_f32_e32 v90, 1.0, v90
	v_pk_fma_f32 v[58:59], v[228:229], v[66:67], v[58:59]
	v_pk_mul_f32 v[108:109], v[108:109], v[112:113]
	v_pk_fma_f32 v[58:59], v[234:235], v[78:79], v[58:59]
	v_rcp_f32_e32 v112, v90
	v_pk_fma_f32 v[114:115], v[242:243], v[72:73], v[58:59]
	v_add_f32_e32 v90, 1.0, v110
	v_mul_f32_e32 v58, 0xbfb8aa3b, v114
	v_rcp_f32_e32 v113, v90
	v_exp_f32_e32 v90, v58
	v_mul_f32_e32 v58, 0xbfb8aa3b, v115
	v_exp_f32_e32 v110, v58
	v_pk_mul_f32 v[58:59], v[62:63], v[112:113]
	v_add_f32_e32 v62, 1.0, v90
	v_rcp_f32_e32 v62, v62
	v_add_f32_e32 v63, 1.0, v110
	v_rcp_f32_e32 v63, v63
	v_pk_fma_f32 v[68:69], v[224:225], v[68:69], 0 op_sel_hi:[1,1,0]
	v_pk_mul_f32 v[112:113], v[58:59], v[58:59]
	v_pk_fma_f32 v[68:69], v[230:231], v[74:75], v[68:69]
	v_pk_mul_f32 v[62:63], v[114:115], v[62:63]
	v_pk_fma_f32 v[68:69], v[238:239], v[76:77], v[68:69]
	v_add_f32_e32 v122, v112, v113
	v_pk_fma_f32 v[68:69], v[244:245], v[60:61], v[68:69]
	v_pk_mul_f32 v[112:113], v[62:63], v[62:63]
	v_mul_f32_e32 v110, 0xbfb8aa3b, v68
	v_add_f32_e32 v123, v112, v113
	v_exp_f32_e32 v110, v110
	v_mul_f32_e32 v112, 0xbfb8aa3b, v69
	v_exp_f32_e32 v113, v112
	v_pk_fma_f32 v[66:67], v[222:223], v[66:67], 0 op_sel_hi:[1,1,0]
	v_add_f32_e32 v110, 1.0, v110
	v_pk_fma_f32 v[66:67], v[228:229], v[78:79], v[66:67]
	v_rcp_f32_e32 v112, v110
	v_pk_fma_f32 v[66:67], v[234:235], v[72:73], v[66:67]
	v_add_f32_e32 v110, 1.0, v113
	v_pk_fma_f32 v[114:115], v[242:243], v[54:55], v[66:67]
	v_rcp_f32_e32 v113, v110
	v_mul_f32_e32 v66, 0xbfb8aa3b, v114
	v_exp_f32_e32 v110, v66
	v_mul_f32_e32 v66, 0xbfb8aa3b, v115
	v_exp_f32_e32 v124, v66
	v_pk_mul_f32 v[66:67], v[68:69], v[112:113]
	v_add_f32_e32 v68, 1.0, v110
	v_pk_mul_f32 v[112:113], v[66:67], v[66:67]
	v_add_f32_e32 v69, 1.0, v124
	v_pk_fma_f32 v[84:85], v[226:227], v[84:85], 0 op_sel_hi:[0,1,0]
	v_rcp_f32_e32 v68, v68
	v_rcp_f32_e32 v69, v69
	v_add_f32_e32 v124, v112, v113
	v_pk_mov_b32 v[112:113], v[86:87], v[70:71] op_sel:[1,0]
	v_pk_fma_f32 v[84:85], v[232:233], v[86:87], v[84:85] op_sel_hi:[0,1,1]
	v_pk_fma_f32 v[84:85], v[240:241], v[112:113], v[84:85] op_sel_hi:[0,1,1]
	v_pk_fma_f32 v[84:85], v[246:247], v[70:71], v[84:85] op_sel_hi:[0,1,1]
	v_mul_f32_e32 v86, 0xbfb8aa3b, v84
	v_pk_mul_f32 v[68:69], v[114:115], v[68:69]
	v_exp_f32_e32 v114, v86
	v_mul_f32_e32 v86, 0xbfb8aa3b, v85
	v_exp_f32_e32 v115, v86
	v_pk_mul_f32 v[86:87], v[68:69], v[68:69]
	v_add_f32_e32 v114, 1.0, v114
	v_pk_fma_f32 v[80:81], v[226:227], v[80:81], 0 op_sel:[1,0,0] op_sel_hi:[1,1,0]
	v_add_f32_e32 v115, 1.0, v115
	v_rcp_f32_e32 v114, v114
	v_rcp_f32_e32 v115, v115
	v_add_f32_e32 v125, v86, v87
	v_pk_mov_b32 v[86:87], v[82:83], v[64:65] op_sel:[1,0]
	v_pk_fma_f32 v[80:81], v[232:233], v[82:83], v[80:81] op_sel:[1,0,0]
	v_pk_mul_f32 v[84:85], v[84:85], v[114:115]
	v_pk_fma_f32 v[80:81], v[240:241], v[86:87], v[80:81] op_sel:[1,0,0]
	s_mul_i32 s1, s76, 0x12000
	v_pk_fma_f32 v[80:81], v[246:247], v[64:65], v[80:81] op_sel:[1,0,0]
	s_mul_hi_i32 s0, s76, 0x12000
	v_mul_f32_e32 v82, 0xbfb8aa3b, v80
	v_exp_f32_e32 v114, v82
	v_mul_f32_e32 v82, 0xbfb8aa3b, v81
	v_exp_f32_e32 v115, v82
	s_add_u32 s78, s40, s1
	s_addc_u32 s79, s41, s0
	s_mul_i32 s0, s82, 0x440
	v_readlane_b32 s82, v95, s55
	v_readlane_b32 s83, v95, s33
	v_pk_fma_f32 v[74:75], v[224:225], v[74:75], 0 op_sel_hi:[1,1,0]
	v_pk_fma_f32 v[78:79], v[222:223], v[78:79], 0 op_sel_hi:[1,1,0]
	v_pk_mul_f32 v[82:83], v[84:85], s[82:83]
	v_add_f32_e32 v84, 1.0, v114
	v_rcp_f32_e32 v114, v84
	v_add_f32_e32 v84, 1.0, v115
	v_rcp_f32_e32 v115, v84
	v_pk_fma_f32 v[74:75], v[230:231], v[76:77], v[74:75]
	v_cvt_pk_bf16_f32 v84, v82, v83
	v_pk_fma_f32 v[74:75], v[238:239], v[60:61], v[74:75]
	v_pk_mul_f32 v[80:81], v[80:81], v[114:115]
	v_pk_fma_f32 v[74:75], v[244:245], v[46:47], v[74:75]
	v_pk_mul_f32 v[80:81], v[80:81], s[82:83]
	v_mul_f32_e32 v82, 0xbfb8aa3b, v74
	v_mul_f32_e32 v114, 0xbfb8aa3b, v75
	v_exp_f32_e32 v82, v82
	v_exp_f32_e32 v114, v114
	v_cvt_pk_bf16_f32 v115, v80, v81
	v_pk_fma_f32 v[78:79], v[228:229], v[72:73], v[78:79]
	v_add_f32_e32 v80, 1.0, v82
	v_add_f32_e32 v81, 1.0, v114
	v_rcp_f32_e32 v80, v80
	v_rcp_f32_e32 v81, v81
	v_pk_fma_f32 v[78:79], v[234:235], v[54:55], v[78:79]
	v_and_b32_e32 v118, 32, v215
	v_pk_fma_f32 v[78:79], v[242:243], v[32:33], v[78:79]
	v_pk_mul_f32 v[74:75], v[74:75], v[80:81]
	v_cmp_eq_u32_e32 vcc, 0, v118
	v_pk_mul_f32 v[80:81], v[74:75], v[74:75]
	v_mul_f32_e32 v118, 0xbfb8aa3b, v79
	v_add_f32_e32 v80, v80, v81
	v_mul_f32_e32 v81, 0xbfb8aa3b, v78
	v_exp_f32_e32 v81, v81
	v_exp_f32_e32 v118, v118
	v_add_u32_e32 v89, 0x48, v93
	v_or_b32_e32 v126, 2, v92
	v_add_u32_e32 v83, v126, v89
	v_lshl_add_u32 v114, v83, 1, s12
	v_cndmask_b32_e32 v83, v80, v119, vcc
	v_cndmask_b32_e32 v80, v119, v80, vcc
	ds_bpermute_b32 v119, v105, v80
	v_add_f32_e32 v80, 1.0, v81
	v_add_f32_e32 v81, 1.0, v118
	v_rcp_f32_e32 v80, v80
	v_rcp_f32_e32 v81, v81
	v_pk_fma_f32 v[76:77], v[224:225], v[76:77], 0 op_sel_hi:[1,1,0]
	s_waitcnt lgkmcnt(0)
	v_add_f32_e32 v118, v83, v119
	v_pk_fma_f32 v[76:77], v[230:231], v[60:61], v[76:77]
	v_pk_mul_f32 v[78:79], v[78:79], v[80:81]
	v_pk_fma_f32 v[76:77], v[238:239], v[46:47], v[76:77]
	v_pk_mul_f32 v[80:81], v[78:79], v[78:79]
	v_pk_fma_f32 v[76:77], v[244:245], v[48:49], v[76:77]
	v_add_f32_e32 v80, v80, v81
	v_cndmask_b32_e32 v119, v80, v116, vcc
	v_cndmask_b32_e32 v80, v116, v80, vcc
	v_mul_f32_e32 v81, 0xbfb8aa3b, v76
	v_mul_f32_e32 v116, 0xbfb8aa3b, v77
	v_exp_f32_e32 v81, v81
	v_exp_f32_e32 v116, v116
	v_pk_mul_f32 v[108:109], v[108:109], s[2:3]
	v_add_lshl_u32 v121, v92, v89, 1
	v_cvt_pk_bf16_f32 v108, v108, v109
	v_add_u32_e32 v109, s12, v121
	v_add_u32_e32 v82, 0, v121
	ds_bpermute_b32 v121, v105, v80
	v_add_f32_e32 v80, 1.0, v81
	v_add_f32_e32 v81, 1.0, v116
	v_rcp_f32_e32 v80, v80
	v_rcp_f32_e32 v81, v81
	v_pk_fma_f32 v[72:73], v[222:223], v[72:73], 0 op_sel_hi:[1,1,0]
	s_waitcnt lgkmcnt(0)
	v_add_f32_e32 v116, v119, v121
	v_pk_fma_f32 v[72:73], v[228:229], v[54:55], v[72:73]
	v_pk_mul_f32 v[76:77], v[76:77], v[80:81]
	v_pk_fma_f32 v[72:73], v[234:235], v[32:33], v[72:73]
	v_pk_mul_f32 v[80:81], v[76:77], v[76:77]
	v_pk_fma_f32 v[72:73], v[242:243], v[34:35], v[72:73]
	v_add_f32_e32 v119, v80, v81
	v_mul_f32_e32 v81, 0xbfb8aa3b, v72
	v_mul_f32_e32 v121, 0xbfb8aa3b, v73
	v_exp_f32_e32 v81, v81
	v_exp_f32_e32 v121, v121
	v_cndmask_b32_e32 v80, v117, v119, vcc
	v_add_u32_e32 v127, v126, v93
	ds_bpermute_b32 v126, v105, v80
	v_add_f32_e32 v80, 1.0, v81
	v_add_f32_e32 v81, 1.0, v121
	v_rcp_f32_e32 v80, v80
	v_rcp_f32_e32 v81, v81
	v_pk_fma_f32 v[112:113], v[226:227], v[112:113], 0 op_sel_hi:[0,1,0]
	v_cndmask_b32_e32 v117, v119, v117, vcc
	s_waitcnt lgkmcnt(0)
	v_add_f32_e32 v117, v117, v126
	v_pk_mul_f32 v[80:81], v[72:73], v[80:81]
	v_pk_fma_f32 v[60:61], v[224:225], v[60:61], 0 op_sel_hi:[1,1,0]
	v_pk_mul_f32 v[72:73], v[80:81], v[80:81]
	v_pk_fma_f32 v[60:61], v[230:231], v[46:47], v[60:61]
	v_add_f32_e32 v72, v72, v73
	v_cndmask_b32_e32 v121, v72, v120, vcc
	v_cndmask_b32_e32 v120, v120, v72, vcc
	v_pk_mov_b32 v[72:73], v[70:71], v[28:29] op_sel:[1,0]
	v_pk_fma_f32 v[70:71], v[232:233], v[70:71], v[112:113] op_sel_hi:[0,1,1]
	v_pk_fma_f32 v[70:71], v[240:241], v[72:73], v[70:71] op_sel_hi:[0,1,1]
	v_pk_fma_f32 v[70:71], v[246:247], v[28:29], v[70:71] op_sel_hi:[0,1,1]
	v_mul_f32_e32 v112, 0xbfb8aa3b, v71
	v_exp_f32_e32 v112, v112
	v_mul_f32_e32 v113, 0xbfb8aa3b, v70
	v_exp_f32_e32 v126, v113
	v_pk_fma_f32 v[60:61], v[238:239], v[48:49], v[60:61]
	v_add_f32_e32 v112, 1.0, v112
	v_rcp_f32_e32 v113, v112
	v_add_f32_e32 v112, 1.0, v126
	v_rcp_f32_e32 v112, v112
	v_readlane_b32 s92, v95, s4
	v_readlane_b32 s93, v95, s5
	v_pk_fma_f32 v[86:87], v[226:227], v[86:87], 0 op_sel:[1,0,0] op_sel_hi:[1,1,0]
	v_pk_mul_f32 v[70:71], v[70:71], v[112:113]
	v_pk_fma_f32 v[60:61], v[244:245], v[50:51], v[60:61]
	v_pk_mul_f32 v[112:113], v[70:71], s[92:93]
	v_pk_mov_b32 v[70:71], v[64:65], v[24:25] op_sel:[1,0]
	v_pk_fma_f32 v[64:65], v[232:233], v[64:65], v[86:87] op_sel:[1,0,0]
	v_mul_f32_e32 v86, 0xbfb8aa3b, v60
	v_mul_f32_e32 v87, 0xbfb8aa3b, v61
	v_exp_f32_e32 v86, v86
	v_exp_f32_e32 v87, v87
	v_pk_fma_f32 v[54:55], v[222:223], v[54:55], 0 op_sel_hi:[1,1,0]
	v_pk_fma_f32 v[16:17], v[224:225], v[46:47], 0 op_sel_hi:[1,1,0]
	v_add_f32_e32 v86, 1.0, v86
	v_add_f32_e32 v87, 1.0, v87
	v_rcp_f32_e32 v86, v86
	v_rcp_f32_e32 v87, v87
	v_pk_fma_f32 v[8:9], v[222:223], v[32:33], 0 op_sel_hi:[1,1,0]
	v_pk_fma_f32 v[54:55], v[228:229], v[32:33], v[54:55]
	v_pk_fma_f32 v[16:17], v[230:231], v[48:49], v[16:17]
	v_pk_mul_f32 v[60:61], v[60:61], v[86:87]
	v_pk_fma_f32 v[8:9], v[228:229], v[34:35], v[8:9]
	v_pk_mul_f32 v[86:87], v[60:61], v[60:61]
	v_pk_fma_f32 v[54:55], v[234:235], v[34:35], v[54:55]
	v_add_f32_e32 v86, v86, v87
	v_pk_fma_f32 v[16:17], v[238:239], v[50:51], v[16:17]
	v_pk_fma_f32 v[8:9], v[234:235], v[36:37], v[8:9]
	v_cndmask_b32_e32 v87, v122, v86, vcc
	v_pk_fma_f32 v[54:55], v[242:243], v[36:37], v[54:55]
	v_pk_fma_f32 v[16:17], v[244:245], v[52:53], v[16:17]
	v_pk_fma_f32 v[8:9], v[242:243], v[40:41], v[8:9]
	v_lshlrev_b32_e32 v30, 16, v201
	v_and_b32_e32 v26, 0xffff0000, v201
	v_lshl_add_u32 v96, s0, 1, v97
	s_mul_i32 s0, s54, 0x88
	ds_bpermute_b32 v128, v105, v87
	v_cvt_pk_bf16_f32 v129, v112, v113
	v_mul_f32_e32 v112, 0xbfb8aa3b, v54
	v_mul_f32_e32 v113, 0xbfb8aa3b, v55
	v_mul_f32_e32 v18, 0xbfb8aa3b, v16
	v_mul_f32_e32 v19, 0xbfb8aa3b, v17
	v_mul_f32_e32 v10, 0xbfb8aa3b, v8
	v_mul_f32_e32 v11, 0xbfb8aa3b, v9
	v_lshl_add_u32 v106, s0, 1, v97
	v_readlane_b32 s0, v253, 45
	v_exp_f32_e32 v112, v112
	v_exp_f32_e32 v113, v113
	v_exp_f32_e32 v18, v18
	v_exp_f32_e32 v19, v19
	v_exp_f32_e32 v10, v10
	v_exp_f32_e32 v11, v11
	v_lshl_add_u32 v90, s0, 1, v97
	v_readlane_b32 s0, v253, 46
	v_and_b32_e32 v111, 16, v215
	v_cndmask_b32_e32 v86, v86, v122, vcc
	v_lshl_add_u32 v110, s0, 1, v97
	v_readlane_b32 s0, v253, 47
	s_waitcnt lgkmcnt(0)
	v_add_f32_e32 v86, v86, v128
	v_add_f32_e32 v112, 1.0, v112
	v_lshl_add_u32 v83, s0, 1, v97
	v_readlane_b32 s0, v253, 48
	v_add_f32_e32 v113, 1.0, v113
	v_add_f32_e32 v18, 1.0, v18
	v_lshl_add_u32 v119, s0, 1, v97
	v_cmp_eq_u32_e64 s[0:1], 0, v111
	v_add_f32_e32 v19, 1.0, v19
	v_add_f32_e32 v10, 1.0, v10
	v_add_f32_e32 v11, 1.0, v11
	v_cndmask_b32_e64 v111, v86, v118, s[0:1]
	v_cndmask_b32_e64 v86, v118, v86, s[0:1]
	v_rcp_f32_e32 v112, v112
	v_rcp_f32_e32 v113, v113
	v_rcp_f32_e32 v18, v18
	v_rcp_f32_e32 v19, v19
	v_rcp_f32_e32 v10, v10
	v_rcp_f32_e32 v11, v11
	ds_bpermute_b32 v86, v103, v86
	v_pk_mul_f32 v[54:55], v[54:55], v[112:113]
	v_pk_mul_f32 v[16:17], v[16:17], v[18:19]
	v_pk_mul_f32 v[8:9], v[8:9], v[10:11]
	v_pk_mul_f32 v[112:113], v[54:55], v[54:55]
	v_pk_mul_f32 v[18:19], v[16:17], v[16:17]
	v_pk_mul_f32 v[10:11], v[8:9], v[8:9]
	s_waitcnt lgkmcnt(0)
	v_add_f32_e32 v86, v111, v86
	v_add_f32_e32 v111, v112, v113
	v_add_f32_e32 v18, v18, v19
	v_add_f32_e32 v10, v10, v11
	v_cndmask_b32_e32 v112, v111, v123, vcc
	v_cndmask_b32_e32 v111, v123, v111, vcc
	v_cndmask_b32_e32 v19, v18, v124, vcc
	v_cndmask_b32_e32 v18, v124, v18, vcc
	v_cndmask_b32_e32 v11, v125, v10, vcc
	ds_bpermute_b32 v120, v105, v120
	ds_bpermute_b32 v111, v105, v111
	ds_bpermute_b32 v12, v105, v18
	ds_bpermute_b32 v11, v105, v11
	v_cndmask_b32_e32 v10, v10, v125, vcc
	s_waitcnt lgkmcnt(3)
	v_add_f32_e32 v120, v121, v120
	s_waitcnt lgkmcnt(2)
	v_add_f32_e32 v20, v112, v111
	s_waitcnt lgkmcnt(1)
	v_add_f32_e32 v12, v19, v12
	s_waitcnt lgkmcnt(0)
	v_add_f32_e32 v10, v10, v11
	v_cndmask_b32_e64 v21, v20, v116, s[0:1]
	v_cndmask_b32_e64 v20, v116, v20, s[0:1]
	v_cndmask_b32_e64 v13, v117, v12, s[0:1]
	v_cndmask_b32_e64 v11, v120, v10, s[0:1]
	ds_bpermute_b32 v20, v103, v20
	ds_bpermute_b32 v13, v103, v13
	ds_bpermute_b32 v11, v103, v11
	v_and_b32_e32 v104, 8, v215
	v_cndmask_b32_e64 v12, v12, v117, s[0:1]
	v_cndmask_b32_e64 v10, v10, v120, s[0:1]
	s_waitcnt lgkmcnt(2)
	v_add_f32_e32 v14, v21, v20
	s_waitcnt lgkmcnt(1)
	v_add_f32_e32 v12, v12, v13
	v_cmp_eq_u32_e32 vcc, 0, v104
	s_waitcnt lgkmcnt(0)
	v_add_f32_e32 v10, v10, v11
	v_lshlrev_b32_e32 v31, 16, v204
	v_cndmask_b32_e32 v13, v12, v86, vcc
	v_cndmask_b32_e32 v12, v86, v12, vcc
	v_cndmask_b32_e32 v11, v14, v10, vcc
	ds_bpermute_b32 v12, v102, v12
	ds_bpermute_b32 v11, v102, v11
	v_and_b32_e32 v27, 0xffff0000, v204
	v_and_b32_e32 v99, 4, v215
	v_pk_fma_f32 v[64:65], v[240:241], v[70:71], v[64:65] op_sel:[1,0,0]
	v_cndmask_b32_e32 v10, v10, v14, vcc
	v_pk_fma_f32 v[64:65], v[246:247], v[24:25], v[64:65] op_sel:[1,0,0]
	s_waitcnt lgkmcnt(1)
	v_add_f32_e32 v12, v13, v12
	s_waitcnt lgkmcnt(0)
	v_add_f32_e32 v10, v10, v11
	v_cmp_eq_u32_e32 vcc, 0, v99
	v_lshl_add_u32 v85, v127, 1, s12
	v_mul_f32_e32 v127, 0xbfb8aa3b, v65
	v_mul_f32_e32 v118, 0xbfb8aa3b, v64
	v_cndmask_b32_e32 v13, v12, v10, vcc
	v_cndmask_b32_e32 v10, v10, v12, vcc
	v_exp_f32_e32 v127, v127
	v_exp_f32_e32 v118, v118
	ds_bpermute_b32 v12, v101, v10
	v_readlane_b32 s0, v253, 49
	v_add_f32_e32 v87, 1.0, v127
	v_add_f32_e32 v15, 1.0, v118
	v_rcp_f32_e32 v87, v87
	v_rcp_f32_e32 v86, v15
	s_waitcnt lgkmcnt(0)
	v_add_f32_e32 v12, v13, v12
	ds_bpermute_b32 v13, v100, v12
	v_lshl_add_u32 v33, s0, 1, v97
	v_pk_mul_f32 v[10:11], v[64:65], v[86:87]
	v_readlane_b32 s0, v253, 50
	v_pk_mul_f32 v[10:11], v[10:11], s[92:93]
	s_mov_b32 s74, 0x358637bd
	v_cvt_pk_bf16_f32 v23, v10, v11
	s_waitcnt lgkmcnt(0)
	v_add_f32_e32 v10, v12, v13
	ds_bpermute_b32 v11, v98, v10
	v_or_b32_e32 v121, 4, v92
	v_lshl_add_u32 v34, s0, 1, v97
	v_add_u32_e32 v14, v121, v89
	v_lshl_add_u32 v32, v14, 1, s12
	s_waitcnt lgkmcnt(0)
	v_add_f32_e32 v35, v10, v11
	v_mov_b64_e32 v[10:11], s[74:75]
	v_readlane_b32 s1, v35, 0
	v_readlane_b32 s0, v35, 4
	v_readlane_b32 s80, v94, s95
	v_readlane_b32 s81, v94, s54
	v_pk_add_f32 v[12:13], s[0:1], v[10:11] op_sel_hi:[1,0]
	v_readlane_b32 s20, v94, s55
	v_readlane_b32 s21, v94, s33
	v_rsq_f32_e32 v13, v13
	v_rsq_f32_e32 v14, v12
	v_mov_b32_e32 v12, v13
	v_mul_f32_e32 v12, 0x3db504f3, v12
	v_pk_mul_f32 v[12:13], v[44:45], v[12:13] op_sel_hi:[1,0]
	v_readlane_b32 s1, v35, 8
	v_cvt_pk_bf16_f32 v12, v12, v13
	v_readlane_b32 s0, v35, 12
	ds_write_b32 v96, v12 offset:34816
	v_pk_mul_f32 v[14:15], v[38:39], v[14:15] op_sel_hi:[1,0]
	v_pk_add_f32 v[12:13], s[0:1], v[10:11] op_sel_hi:[1,0]
	v_cvt_pk_bf16_f32 v36, v14, v15
	v_readlane_b32 s22, v94, s4
	v_rsq_f32_e32 v13, v13
	v_rsq_f32_e32 v18, v12
	v_mov_b32_e32 v12, v13
	v_mul_f32_e32 v12, 0x3db504f3, v12
	v_pk_mul_f32 v[12:13], v[56:57], v[12:13] op_sel_hi:[1,0]
	v_pk_mul_f32 v[18:19], v[42:43], v[18:19] op_sel_hi:[1,0]
	v_cvt_pk_bf16_f32 v12, v12, v13
	v_cvt_pk_bf16_f32 v37, v18, v19
	ds_write_b32 v106, v12 offset:34816
	v_mov_b32_e32 v12, v14
	v_mov_b32_e32 v13, v18
	v_mov_b32_e32 v18, v15
	v_pk_mul_f32 v[12:13], s[2:3], v[12:13]
	v_pk_mul_f32 v[14:15], s[2:3], v[18:19]
	v_pk_mul_f32 v[20:21], s[80:81], v[12:13]
	v_cvt_pk_bf16_f32 v12, v12, v14
	v_pk_mul_f32 v[18:19], s[80:81], v[14:15]
	ds_write2st64_b32 v96, v36, v12 offset1:68
	v_cvt_pk_bf16_f32 v12, v13, v15
	v_cvt_pk_bf16_f32 v20, v20, v21
	ds_write2st64_b32 v106, v37, v12 offset1:68
	ds_write_b32 v88, v107 offset:52224
	ds_write_b32 v91, v20
	ds_write_b32 v88, v108 offset:52368
	v_cvt_pk_bf16_f32 v12, v18, v19
	v_readlane_b32 s1, v35, 16
	v_readlane_b32 s0, v35, 20
	ds_write_b32 v109, v12
	v_readlane_b32 s23, v94, s5
	v_pk_add_f32 v[12:13], s[0:1], v[10:11] op_sel_hi:[1,0]
	v_add_u32_e32 v126, v121, v93
	v_lshl_add_u32 v22, v126, 1, s12
	v_rsq_f32_e32 v13, v13
	v_rsq_f32_e32 v14, v12
	v_mov_b32_e32 v12, v13
	v_mul_f32_e32 v12, 0x3db504f3, v12
	v_pk_mul_f32 v[12:13], v[62:63], v[12:13] op_sel_hi:[1,0]
	v_readlane_b32 s1, v35, 24
	v_cvt_pk_bf16_f32 v12, v12, v13
	v_readlane_b32 s0, v35, 28
	ds_write_b32 v90, v12 offset:34816
	v_pk_mul_f32 v[14:15], v[58:59], v[14:15] op_sel_hi:[1,0]
	v_pk_add_f32 v[12:13], s[0:1], v[10:11] op_sel_hi:[1,0]
	v_cvt_pk_bf16_f32 v36, v14, v15
	v_readlane_b32 s96, v95, s6
	v_rsq_f32_e32 v13, v13
	v_rsq_f32_e32 v18, v12
	v_mov_b32_e32 v12, v13
	v_mul_f32_e32 v12, 0x3db504f3, v12
	v_pk_mul_f32 v[12:13], v[68:69], v[12:13] op_sel_hi:[1,0]
	v_pk_mul_f32 v[18:19], v[66:67], v[18:19] op_sel_hi:[1,0]
	v_cvt_pk_bf16_f32 v12, v12, v13
	v_cvt_pk_bf16_f32 v37, v18, v19
	ds_write_b32 v110, v12 offset:34816
	v_mov_b32_e32 v12, v14
	v_mov_b32_e32 v13, v18
	v_mov_b32_e32 v18, v15
	v_pk_mul_f32 v[12:13], s[82:83], v[12:13]
	v_pk_mul_f32 v[14:15], s[82:83], v[18:19]
	v_pk_mul_f32 v[20:21], s[20:21], v[12:13]
	v_cvt_pk_bf16_f32 v12, v12, v14
	v_pk_mul_f32 v[18:19], s[20:21], v[14:15]
	ds_write2st64_b32 v90, v36, v12 offset1:68
	v_cvt_pk_bf16_f32 v12, v13, v15
	v_cvt_pk_bf16_f32 v20, v20, v21
	ds_write2st64_b32 v110, v37, v12 offset1:68
	ds_write_b32 v88, v84 offset:52228
	ds_write_b32 v85, v20
	ds_write_b32 v82, v115 offset:52228
	v_cvt_pk_bf16_f32 v12, v18, v19
	v_readlane_b32 s1, v35, 32
	v_readlane_b32 s0, v35, 36
	ds_write_b32 v114, v12
	v_readlane_b32 s97, v95, s7
	v_pk_add_f32 v[12:13], s[0:1], v[10:11] op_sel_hi:[1,0]
	v_readlane_b32 s34, v94, s6
	v_readlane_b32 s35, v94, s7
	v_rsq_f32_e32 v13, v13
	v_rsq_f32_e32 v14, v12
	v_mov_b32_e32 v12, v13
	v_mul_f32_e32 v12, 0x3db504f3, v12
	v_pk_mul_f32 v[12:13], v[78:79], v[12:13] op_sel_hi:[1,0]
	v_pk_mul_f32 v[14:15], v[74:75], v[14:15] op_sel_hi:[1,0]
	v_cvt_pk_bf16_f32 v12, v12, v13
	v_readlane_b32 s1, v35, 40
	v_readlane_b32 s0, v35, 44
	v_cvt_pk_bf16_f32 v18, v14, v15
	ds_write_b32 v83, v12 offset:34816
	v_pk_add_f32 v[12:13], s[0:1], v[10:11] op_sel_hi:[1,0]
	ds_write_b32 v83, v18
	s_mov_b64 s[2:3], -1
	v_rsq_f32_e32 v13, v13
	v_rsq_f32_e32 v18, v12
	v_mov_b32_e32 v12, v13
	v_mul_f32_e32 v12, 0x3db504f3, v12
	v_pk_mul_f32 v[12:13], v[80:81], v[12:13] op_sel_hi:[1,0]
	v_pk_mul_f32 v[18:19], v[76:77], v[18:19] op_sel_hi:[1,0]
	v_cvt_pk_bf16_f32 v12, v12, v13
	v_cvt_pk_bf16_f32 v20, v18, v19
	ds_write_b32 v119, v12 offset:34816
	v_mov_b32_e32 v12, v14
	v_mov_b32_e32 v13, v18
	v_mov_b32_e32 v18, v15
	v_pk_mul_f32 v[12:13], s[92:93], v[12:13]
	v_pk_mul_f32 v[14:15], s[92:93], v[18:19]
	ds_write_b32 v119, v20
	v_pk_mul_f32 v[20:21], s[22:23], v[12:13]
	v_cvt_pk_bf16_f32 v12, v12, v14
	v_pk_mul_f32 v[18:19], s[22:23], v[14:15]
	ds_write_b32 v83, v12 offset:17408
	v_cvt_pk_bf16_f32 v12, v13, v15
	v_cvt_pk_bf16_f32 v20, v20, v21
	ds_write_b32 v119, v12 offset:17408
	ds_write_b32 v88, v129 offset:52232
	ds_write_b32 v22, v20
	ds_write_b32 v82, v23 offset:52232
	v_cvt_pk_bf16_f32 v12, v18, v19
	v_readlane_b32 s1, v35, 48
	v_readlane_b32 s0, v35, 52
	ds_write_b32 v32, v12
	s_nop 0
	v_pk_add_f32 v[12:13], s[0:1], v[10:11] op_sel_hi:[1,0]
	s_nop 0
	s_nop 0
	v_rsq_f32_e32 v13, v13
	v_rsq_f32_e32 v14, v12
	v_mov_b32_e32 v12, v13
	v_mul_f32_e32 v12, 0x3db504f3, v12
	v_pk_mul_f32 v[12:13], v[54:55], v[12:13] op_sel_hi:[1,0]
	v_readlane_b32 s1, v35, 56
	v_readlane_b32 s0, v35, 60
	v_cvt_pk_bf16_f32 v12, v12, v13
	ds_write_b32 v33, v12 offset:34816
	v_pk_add_f32 v[10:11], s[0:1], v[10:11] op_sel_hi:[1,0]
	v_pk_mul_f32 v[14:15], v[60:61], v[14:15] op_sel_hi:[1,0]
	v_cvt_pk_bf16_f32 v18, v14, v15
	v_rsq_f32_e32 v11, v11
	v_rsq_f32_e32 v12, v10
	ds_write_b32 v33, v18
	v_mov_b32_e32 v10, v11
	v_mul_f32_e32 v10, 0x3db504f3, v10
	v_pk_mul_f32 v[8:9], v[8:9], v[10:11] op_sel_hi:[1,0]
	v_pk_mul_f32 v[10:11], v[16:17], v[12:13] op_sel_hi:[1,0]
	v_pk_fma_f32 v[16:17], v[226:227], v[72:73], 0 op_sel_hi:[0,1,0]
	v_cvt_pk_bf16_f32 v12, v10, v11
	ds_write_b32 v34, v12
	v_pk_mov_b32 v[12:13], v[28:29], v[30:31] op_sel:[1,0]
	v_pk_fma_f32 v[16:17], v[232:233], v[28:29], v[16:17] op_sel_hi:[0,1,1]
	v_pk_fma_f32 v[12:13], v[240:241], v[12:13], v[16:17] op_sel_hi:[0,1,1]
	v_pk_fma_f32 v[12:13], v[246:247], v[30:31], v[12:13] op_sel_hi:[0,1,1]
	v_mul_f32_e32 v16, 0xbfb8aa3b, v13
	v_exp_f32_e32 v16, v16
	v_mul_f32_e32 v17, 0xbfb8aa3b, v12
	v_exp_f32_e32 v17, v17
	v_cvt_pk_bf16_f32 v18, v8, v9
	v_add_f32_e32 v8, 1.0, v16
	v_rcp_f32_e32 v9, v8
	v_add_f32_e32 v8, 1.0, v17
	v_rcp_f32_e32 v8, v8
	v_pk_fma_f32 v[0:1], v[226:227], v[70:71], 0 op_sel:[1,0,0] op_sel_hi:[1,1,0]
	ds_write_b32 v34, v18 offset:34816
	v_pk_fma_f32 v[0:1], v[232:233], v[24:25], v[0:1] op_sel:[1,0,0]
	v_pk_mul_f32 v[8:9], v[12:13], v[8:9]
	v_pk_mov_b32 v[12:13], v[24:25], v[26:27] op_sel:[1,0]
	v_pk_mul_f32 v[8:9], v[8:9], s[96:97]
	v_pk_fma_f32 v[0:1], v[240:241], v[12:13], v[0:1] op_sel:[1,0,0]
	v_cvt_pk_bf16_f32 v18, v8, v9
	v_pk_fma_f32 v[0:1], v[246:247], v[26:27], v[0:1] op_sel:[1,0,0]
	v_mov_b32_e32 v8, v14
	v_mul_f32_e32 v2, 0xbfb8aa3b, v1
	v_exp_f32_e32 v4, v2
	v_mul_f32_e32 v2, 0xbfb8aa3b, v0
	v_exp_f32_e32 v6, v2
	v_mov_b32_e32 v9, v10
	v_add_f32_e32 v4, 1.0, v4
	v_rcp_f32_e32 v5, v4
	v_add_f32_e32 v4, 1.0, v6
	v_rcp_f32_e32 v4, v4
	v_pk_mul_f32 v[8:9], s[96:97], v[8:9]
	v_mov_b32_e32 v10, v15
	v_pk_mul_f32 v[2:3], s[34:35], v[8:9]
	v_pk_mul_f32 v[0:1], v[0:1], v[4:5]
	v_or_b32_e32 v16, 6, v92
	v_pk_mul_f32 v[0:1], v[0:1], s[96:97]
	v_cvt_pk_bf16_f32 v6, v2, v3
	v_cvt_pk_bf16_f32 v4, v0, v1
	v_pk_mul_f32 v[0:1], s[96:97], v[10:11]
	v_add_u32_e32 v17, v16, v93
	v_pk_mul_f32 v[2:3], s[34:35], v[0:1]
	v_cvt_pk_bf16_f32 v0, v8, v0
	v_add_u32_e32 v12, v16, v89
	ds_write_b32 v33, v0 offset:17408
	v_cvt_pk_bf16_f32 v0, v9, v1
	v_lshl_add_u32 v7, v17, 1, s12
	ds_write_b32 v34, v0 offset:17408
	ds_write_b32 v88, v18 offset:52236
	ds_write_b32 v7, v6
	ds_write_b32 v82, v4 offset:52236
	v_cvt_pk_bf16_f32 v0, v2, v3
	v_lshl_add_u32 v1, v12, 1, s12
	ds_write_b32 v1, v0
	s_waitcnt lgkmcnt(0)
	s_barrier
	s_cmp_lg_u32 s95, 0
	s_cbranch_scc1 .Lgpf_done_next
	v_readlane_b32 s99, v253, 10
	s_nop 0
	s_add_i32 s99, s76, s99
	s_cmpk_lt_i32 s99, 0x800
	s_cbranch_scc0 .Lgpf_done_next
	v_readlane_b32 s100, v253, 17
	s_lshr_b32 s0, s99, 8
	s_lshl_b32 s0, s0, 12
	s_and_b32 s1, s99, 63
	s_lshl_b32 s101, s1, 6
	s_add_i32 s0, s0, s101
	s_or_b32 s1, s1, s100
	s_bfe_u32 s101, s99, 0x20006
	v_add_u32_e32 v219, s0, v237
	v_lshlrev_b32_e32 v219, 5, v219
	s_lshl_b32 s99, s101, 2
	v_add_u32_e32 v219, s99, v219
	s_lshl_b32 s100, s100, 3
	s_add_i32 s0, s0, s100
	s_lshl_b32 s0, s0, 10
	s_lshl_b32 s101, s101, 8
	s_add_i32 s0, s0, s101
	v_lshlrev_b32_e32 v217, 2, v237
	v_add_u32_e32 v217, s0, v217
	v_add_u32_e32 v218, 0x1000, v217
	s_add_u32 s100, s88, 0x200000
	s_addc_u32 s101, s89, 0
	s_cmp_eq_u32 s1, 0
	s_cbranch_scc1 .Lgpf_zero_next
	global_load_dword v172, v217, s[44:45] offset:-3072 nt
	global_load_dword v173, v217, s[68:69] offset:-3072 nt
	global_load_dword v174, v217, s[72:73] offset:-3072 nt
	global_load_dword v175, v217, s[44:45] offset:-2048 nt
	global_load_dword v176, v217, s[68:69] offset:-2048 nt
	global_load_dword v177, v217, s[72:73] offset:-2048 nt
	global_load_dword v178, v217, s[44:45] offset:-1024 nt
	global_load_dword v179, v217, s[68:69] offset:-1024 nt
	global_load_dword v180, v217, s[72:73] offset:-1024 nt
	s_branch .Lgpf_rest_next
